# P1: first half K-iteration of each unit peeled, first MFMA per accumulator takes C=0 instead of 128 v_mov zeroing
# baseline (speedup 1.0000x reference)
; #define PG8_STAGE(bufoff, gbase, voff) do { _Pragma("unroll") for (int _i = 0; _i < 2; ++_i) \
;         __builtin_amdgcn_global_load_lds((const unsigned*)((const char*)(gbase) + (voff)[_i]), (PG8_LAS unsigned*)(lds + (bufoff) + ldsw + _i * 8192), 16, 0, 0); } while (0)
; #define PG8_LDA(dst, b, h) do { _Pragma("unroll") for (int m = 0; m < 4; ++m) _Pragma("unroll") for (int k = 0; k < 2; ++k) dst[m][k] = *(const PG8_LAS bf16x8*)(lds + PG8_SA(b, h) + aoff + m * 2048 + k * 1024); } while (0)
; #define PG8_LDB(dst, b, h) do { _Pragma("unroll") for (int n = 0; n < 2; ++n) _Pragma("unroll") for (int k = 0; k < 2; ++k) dst[n][k] = *(const PG8_LAS bf16x8*)(lds + PG8_SB(b, h) + boff + n * 2048 + k * 1024); } while (0)
; #define PG8_WAIT_V(n) asm volatile("s_waitcnt vmcnt(" #n ")" ::: "memory")
; #define PG8_WAIT_L(n) asm volatile("s_waitcnt lgkmcnt(" #n ")" ::: "memory")
; template <class Epi, class Sched, bool ALIGN_EPI = false, bool SP2 = false>
; __device__ __forceinline__ void gemm_phase(PG8_LAS unsigned char* lds, const Gemm g, const Sched& S, const Epi& E) {
;     ...
;         const bool has_next = S.next(ui + 1, nxt);
;         const char* nA = has_next ? (const char*)g.A + (size_t)nxt.pm * tstep : cA; const char* nB = has_next ? (const char*)g.Bt + (size_t)nxt.pn * tstep : cB;
;         for (int t = 0; t < nt; t += 2) {
;             const bool last = (t == nt - 2);
;             const char* a1 = cA + (size_t)(t + 1) * kstep;
;             const char* a2 = last ? nA : cA + (size_t)(t + 2) * kstep; const char* b2 = last ? nB : cB + (size_t)(t + 2) * kstep;
;             const char* a3 = a2 + kstep; const char* b3 = b2 + kstep;
;             if (last && has_next) S.a_ready(nxt);
;             if constexpr (Epi::HAS_MID) { if (t != 0 && (t & (Epi::MID_EVERY - 1)) == 0) E.mid(acc, cur, t / Epi::MID_EVERY, wr, wc, fr, fq); }
;             if constexpr (SP2) {
;             PG8_LDB(B0, 0, 0); PG8_LDB(B1, 0, 1); PG8_SCHED; PG8_LDA(At, 0, 0); PG8_STAGE(PG8_SA(1, 1), a1 + hstep, voffA);
;             PG8_WAIT_V(8); PG8_WAIT_L(0); PG8_BAR; PG8_MMA(0, 0, At, B0); PG8_MMA(0, 1, At, B1); PG8_BAR; PG8_SCHED;
;             PG8_LDA(At, 0, 1); PG8_STAGE(PG8_SB(0, 0), b2, voffB); PG8_STAGE(PG8_SB(0, 1), b2 + hstep, voffB); PG8_STAGE(PG8_SA(0, 0), a2, voffA);
;             PG8_WAIT_V(8); PG8_WAIT_L(0); PG8_BAR; PG8_MMA(1, 0, At, B0); PG8_MMA(1, 1, At, B1); PG8_BAR; PG8_SCHED;
.LBB0_152:
	s_ashr_i32 s41, s40, 31
	s_lshl_b64 s[42:43], s[40:41], 21
	s_add_u32 s42, s54, s42
	s_addc_u32 s43, s55, s43
	s_and_b64 s[44:45], s[10:11], exec
	s_cselect_b32 s41, s43, s13
	s_cselect_b32 s50, s42, s12
	s_ashr_i32 s39, s38, 31
	s_lshl_b64 s[44:45], s[38:39], 21
	s_add_u32 s44, s56, s44
	s_addc_u32 s45, s57, s45
	s_and_b64 s[48:49], s[10:11], exec
	s_cselect_b32 s39, s45, s47
	s_cselect_b32 s51, s44, s46
	s_add_u32 s12, s12, 0x100080
	s_addc_u32 s13, s13, 0
	s_add_u32 s52, s46, 0x100
	s_addc_u32 s53, s47, 0
	s_mov_b32 s80, -2
	s_add_u32 s46, s12, 0xfff00080
	s_addc_u32 s47, s13, -1
	s_add_i32 s81, 0, 0x10000
	s_cmp_eq_u32 s80, 60
	s_cselect_b32 s49, s41, s47
	s_cselect_b32 s48, s50, s46
	s_cselect_b32 s47, s39, s53
	s_cselect_b32 s46, s51, s52
	s_add_i32 s84, 0, 0x14000
	v_add_u32_e32 v158, s81, v190
	v_add_u32_e32 v174, s84, v190
	s_waitcnt lgkmcnt(0)
	ds_read_b128 v[146:149], v158
	ds_read_b128 v[150:153], v158 offset:1024
	ds_read_b128 v[154:157], v158 offset:2048
	ds_read_b128 v[158:161], v158 offset:3072
	ds_read_b128 v[162:165], v174
	ds_read_b128 v[166:169], v174 offset:1024
	ds_read_b128 v[170:173], v174 offset:2048
	ds_read_b128 v[174:177], v174 offset:3072
	v_lshl_add_u64 v[194:195], s[12:13], 0, v[142:143]
	s_add_i32 m0, s59, 0xc000
	ds_read_b128 v[178:181], v196
	ds_read_b128 v[182:185], v196 offset:1024
	ds_read_b128 v[186:189], v196 offset:2048
	ds_read_b128 v[198:201], v196 offset:3072
	ds_read_b128 v[202:205], v196 offset:4096
	ds_read_b128 v[206:209], v196 offset:5120
	ds_read_b128 v[210:213], v196 offset:6144
	ds_read_b128 v[214:217], v196 offset:7168
	global_load_lds_dwordx4 v[194:195], off
	v_lshl_add_u64 v[194:195], s[12:13], 0, v[144:145]
	s_add_i32 m0, s59, 0xe000
	s_nop 0
	global_load_lds_dwordx4 v[194:195], off
	s_waitcnt vmcnt(8)
	s_waitcnt lgkmcnt(0)
	s_barrier
	s_setprio 1
	s_waitcnt lgkmcnt(0)
	v_mfma_f32_16x16x32_bf16 v[128:131], v[146:149], v[178:181], 0
	v_mfma_f32_16x16x32_bf16 v[124:127], v[154:157], v[178:181], 0
	v_mfma_f32_16x16x32_bf16 v[112:115], v[146:149], v[186:189], 0
	v_mfma_f32_16x16x32_bf16 v[108:111], v[154:157], v[186:189], 0
	v_mfma_f32_16x16x32_bf16 v[96:99], v[146:149], v[202:205], 0
	v_mfma_f32_16x16x32_bf16 v[92:95], v[154:157], v[202:205], 0
	v_mfma_f32_16x16x32_bf16 v[80:83], v[146:149], v[210:213], 0
	v_mfma_f32_16x16x32_bf16 v[76:79], v[154:157], v[210:213], 0
	v_mfma_f32_16x16x32_bf16 v[128:131], v[150:153], v[182:185], v[128:131]
	v_mfma_f32_16x16x32_bf16 v[124:127], v[158:161], v[182:185], v[124:127]
	v_mfma_f32_16x16x32_bf16 v[112:115], v[150:153], v[198:201], v[112:115]
	v_mfma_f32_16x16x32_bf16 v[108:111], v[158:161], v[198:201], v[108:111]
	v_mfma_f32_16x16x32_bf16 v[96:99], v[150:153], v[206:209], v[96:99]
	v_mfma_f32_16x16x32_bf16 v[92:95], v[158:161], v[206:209], v[92:95]
	v_mfma_f32_16x16x32_bf16 v[80:83], v[150:153], v[214:217], v[80:83]
	v_mfma_f32_16x16x32_bf16 v[76:79], v[158:161], v[214:217], v[76:79]
	s_setprio 0
	s_setprio 1
	v_mfma_f32_16x16x32_bf16 v[120:123], v[162:165], v[178:181], 0
	v_mfma_f32_16x16x32_bf16 v[116:119], v[170:173], v[178:181], 0
	v_mfma_f32_16x16x32_bf16 v[104:107], v[162:165], v[186:189], 0
	v_mfma_f32_16x16x32_bf16 v[100:103], v[170:173], v[186:189], 0
	v_mfma_f32_16x16x32_bf16 v[88:91], v[162:165], v[202:205], 0
	v_mfma_f32_16x16x32_bf16 v[84:87], v[170:173], v[202:205], 0
	v_mfma_f32_16x16x32_bf16 v[72:75], v[162:165], v[210:213], 0
	v_mfma_f32_16x16x32_bf16 v[68:71], v[170:173], v[210:213], 0
	v_mfma_f32_16x16x32_bf16 v[120:123], v[166:169], v[182:185], v[120:123]
	v_mfma_f32_16x16x32_bf16 v[116:119], v[174:177], v[182:185], v[116:119]
	v_mfma_f32_16x16x32_bf16 v[104:107], v[166:169], v[198:201], v[104:107]
	v_mfma_f32_16x16x32_bf16 v[100:103], v[174:177], v[198:201], v[100:103]
	v_mfma_f32_16x16x32_bf16 v[88:91], v[166:169], v[206:209], v[88:91]
	v_mfma_f32_16x16x32_bf16 v[84:87], v[174:177], v[206:209], v[84:87]
	v_mfma_f32_16x16x32_bf16 v[72:75], v[166:169], v[214:217], v[72:75]
	v_mfma_f32_16x16x32_bf16 v[68:71], v[174:177], v[214:217], v[68:71]
	s_setprio 0
	s_barrier
; #define PG8_STAGE(bufoff, gbase, voff) do { _Pragma("unroll") for (int _i = 0; _i < 2; ++_i) \
;         __builtin_amdgcn_global_load_lds((const unsigned*)((const char*)(gbase) + (voff)[_i]), (PG8_LAS unsigned*)(lds + (bufoff) + ldsw + _i * 8192), 16, 0, 0); } while (0)
; #define PG8_LDA(dst, b, h) do { _Pragma("unroll") for (int m = 0; m < 4; ++m) _Pragma("unroll") for (int k = 0; k < 2; ++k) dst[m][k] = *(const PG8_LAS bf16x8*)(lds + PG8_SA(b, h) + aoff + m * 2048 + k * 1024); } while (0)
; #define PG8_MMA(ai, bj, At, Bt) do { __builtin_amdgcn_s_setprio(1); _Pragma("unroll") for (int m = 0; m < 4; ++m) _Pragma("unroll") for (int n = 0; n < 2; ++n) _Pragma("unroll") for (int k = 0; k < 2; ++k) \
;         acc[ai][bj][m][n] = __builtin_amdgcn_mfma_f32_16x16x32_bf16(Bt[n][k], At[m][k], acc[ai][bj][m][n], 0, 0, 0); __builtin_amdgcn_s_setprio(0); } while (0)
; #define PG8_WAIT_V(n) asm volatile("s_waitcnt vmcnt(" #n ")" ::: "memory")
; #define PG8_WAIT_L(n) asm volatile("s_waitcnt lgkmcnt(" #n ")" ::: "memory")
; #define PG8_BAR __builtin_amdgcn_s_barrier()
; #define PG8_SCHED __builtin_amdgcn_sched_barrier(0)
; template <class Epi, class Sched, bool ALIGN_EPI = false, bool SP2 = false>
; __device__ __forceinline__ void gemm_phase(PG8_LAS unsigned char* lds, const Gemm g, const Sched& S, const Epi& E) {
;     ...
;             PG8_LDA(At, 0, 1); PG8_STAGE(PG8_SB(0, 0), b2, voffB); PG8_STAGE(PG8_SB(0, 1), b2 + hstep, voffB); PG8_STAGE(PG8_SA(0, 0), a2, voffA);
;             PG8_WAIT_V(8); PG8_WAIT_L(0); PG8_BAR; PG8_MMA(1, 0, At, B0); PG8_MMA(1, 1, At, B1); PG8_BAR; PG8_SCHED;
	s_add_i32 s81, s81, s58
	v_lshl_add_u64 v[194:195], s[46:47], 0, v[2:3]
	s_mov_b32 m0, s81
	ds_read_b128 v[178:181], v196 offset:16384
	ds_read_b128 v[182:185], v196 offset:17408
	ds_read_b128 v[186:189], v196 offset:18432
	ds_read_b128 v[198:201], v196 offset:19456
	ds_read_b128 v[202:205], v196 offset:20480
	ds_read_b128 v[206:209], v196 offset:21504
	ds_read_b128 v[210:213], v196 offset:22528
	ds_read_b128 v[214:217], v196 offset:23552
	global_load_lds_dwordx4 v[194:195], off
	s_add_i32 m0, s81, 0x2000
	s_add_u32 s82, s46, 0x100000
	v_lshl_add_u64 v[222:223], s[46:47], 0, v[132:133]
	s_addc_u32 s83, s47, 0
	s_add_i32 s81, s84, s58
	global_load_lds_dwordx4 v[222:223], off
	v_lshl_add_u64 v[232:233], s[82:83], 0, v[2:3]
	s_mov_b32 m0, s81
	v_lshl_add_u64 v[234:235], s[48:49], 0, v[134:135]
	global_load_lds_dwordx4 v[232:233], off
	v_lshl_add_u64 v[232:233], s[82:83], 0, v[132:133]
	s_add_i32 m0, s81, 0x2000
	s_nop 0
	global_load_lds_dwordx4 v[232:233], off
	v_lshl_add_u64 v[232:233], s[48:49], 0, v[136:137]
	s_mov_b32 m0, s59
	s_nop 0
	global_load_lds_dwordx4 v[232:233], off
	s_mov_b32 m0, s60
	s_nop 0
	global_load_lds_dwordx4 v[234:235], off
	s_waitcnt vmcnt(8)
	s_waitcnt lgkmcnt(0)
	s_barrier
	s_setprio 1
	s_waitcnt lgkmcnt(0)
	v_mfma_f32_16x16x32_bf16 v[64:67], v[146:149], v[178:181], 0
	v_mfma_f32_16x16x32_bf16 v[60:63], v[154:157], v[178:181], 0
	v_mfma_f32_16x16x32_bf16 v[48:51], v[146:149], v[186:189], 0
	v_mfma_f32_16x16x32_bf16 v[44:47], v[154:157], v[186:189], 0
	v_mfma_f32_16x16x32_bf16 v[32:35], v[146:149], v[202:205], 0
	v_mfma_f32_16x16x32_bf16 v[28:31], v[154:157], v[202:205], 0
	v_mfma_f32_16x16x32_bf16 v[16:19], v[146:149], v[210:213], 0
	v_mfma_f32_16x16x32_bf16 v[12:15], v[154:157], v[210:213], 0
	v_mfma_f32_16x16x32_bf16 v[64:67], v[150:153], v[182:185], v[64:67]
	v_mfma_f32_16x16x32_bf16 v[60:63], v[158:161], v[182:185], v[60:63]
	v_mfma_f32_16x16x32_bf16 v[48:51], v[150:153], v[198:201], v[48:51]
	v_mfma_f32_16x16x32_bf16 v[44:47], v[158:161], v[198:201], v[44:47]
	v_mfma_f32_16x16x32_bf16 v[32:35], v[150:153], v[206:209], v[32:35]
	v_mfma_f32_16x16x32_bf16 v[28:31], v[158:161], v[206:209], v[28:31]
	v_mfma_f32_16x16x32_bf16 v[16:19], v[150:153], v[214:217], v[16:19]
	v_mfma_f32_16x16x32_bf16 v[12:15], v[158:161], v[214:217], v[12:15]
	s_setprio 0
	s_setprio 1
	v_mfma_f32_16x16x32_bf16 v[56:59], v[162:165], v[178:181], 0
	v_mfma_f32_16x16x32_bf16 v[52:55], v[170:173], v[178:181], 0
	v_mfma_f32_16x16x32_bf16 v[40:43], v[162:165], v[186:189], 0
	v_mfma_f32_16x16x32_bf16 v[36:39], v[170:173], v[186:189], 0
	v_mfma_f32_16x16x32_bf16 v[24:27], v[162:165], v[202:205], 0
	v_mfma_f32_16x16x32_bf16 v[20:23], v[170:173], v[202:205], 0
	v_mfma_f32_16x16x32_bf16 v[8:11], v[162:165], v[210:213], 0
	v_mfma_f32_16x16x32_bf16 v[4:7], v[170:173], v[210:213], 0
	v_mfma_f32_16x16x32_bf16 v[56:59], v[166:169], v[182:185], v[56:59]
	v_mfma_f32_16x16x32_bf16 v[52:55], v[174:177], v[182:185], v[52:55]
	v_mfma_f32_16x16x32_bf16 v[40:43], v[166:169], v[198:201], v[40:43]
	v_mfma_f32_16x16x32_bf16 v[36:39], v[174:177], v[198:201], v[36:39]
	v_mfma_f32_16x16x32_bf16 v[24:27], v[166:169], v[206:209], v[24:27]
	v_mfma_f32_16x16x32_bf16 v[20:23], v[174:177], v[206:209], v[20:23]
	v_mfma_f32_16x16x32_bf16 v[8:11], v[166:169], v[214:217], v[8:11]
	v_mfma_f32_16x16x32_bf16 v[4:7], v[174:177], v[214:217], v[4:7]
	s_setprio 0
	s_barrier
	s_branch .Lp1_kloop_mid

; #define PG8_STAGE(bufoff, gbase, voff) do { _Pragma("unroll") for (int _i = 0; _i < 2; ++_i) \
;         __builtin_amdgcn_global_load_lds((const unsigned*)((const char*)(gbase) + (voff)[_i]), (PG8_LAS unsigned*)(lds + (bufoff) + ldsw + _i * 8192), 16, 0, 0); } while (0)
; #define PG8_LDA(dst, b, h) do { _Pragma("unroll") for (int m = 0; m < 4; ++m) _Pragma("unroll") for (int k = 0; k < 2; ++k) dst[m][k] = *(const PG8_LAS bf16x8*)(lds + PG8_SA(b, h) + aoff + m * 2048 + k * 1024); } while (0)
; #define PG8_LDB(dst, b, h) do { _Pragma("unroll") for (int n = 0; n < 2; ++n) _Pragma("unroll") for (int k = 0; k < 2; ++k) dst[n][k] = *(const PG8_LAS bf16x8*)(lds + PG8_SB(b, h) + boff + n * 2048 + k * 1024); } while (0)
; #define PG8_MMA(ai, bj, At, Bt) do { __builtin_amdgcn_s_setprio(1); _Pragma("unroll") for (int m = 0; m < 4; ++m) _Pragma("unroll") for (int n = 0; n < 2; ++n) _Pragma("unroll") for (int k = 0; k < 2; ++k) \
;         acc[ai][bj][m][n] = __builtin_amdgcn_mfma_f32_16x16x32_bf16(Bt[n][k], At[m][k], acc[ai][bj][m][n], 0, 0, 0); __builtin_amdgcn_s_setprio(0); } while (0)
; #define PG8_WAIT_V(n) asm volatile("s_waitcnt vmcnt(" #n ")" ::: "memory")
; #define PG8_WAIT_L(n) asm volatile("s_waitcnt lgkmcnt(" #n ")" ::: "memory")
; #define PG8_BAR __builtin_amdgcn_s_barrier()
; #define PG8_SCHED __builtin_amdgcn_sched_barrier(0)
; template <class Epi, class Sched, bool ALIGN_EPI = false, bool SP2 = false>
; __device__ __forceinline__ void gemm_phase(PG8_LAS unsigned char* lds, const Gemm g, const Sched& S, const Epi& E) {
;     ...
;             PG8_LDB(B0, 1, 0); PG8_LDB(B1, 1, 1); PG8_SCHED; PG8_LDA(At, 1, 0); PG8_STAGE(PG8_SA(0, 1), a2 + hstep, voffA);
;             PG8_WAIT_V(8); PG8_WAIT_L(0); PG8_BAR; PG8_MMA(0, 0, At, B0); PG8_MMA(0, 1, At, B1); PG8_BAR; PG8_SCHED;
.Lp1_kloop_mid:
	s_add_i32 s81, 0, 0x18000
	s_add_i32 s82, 0, 0x1c000
	v_add_u32_e32 v158, s81, v190
	v_add_u32_e32 v174, s82, v190
	ds_read_b128 v[146:149], v158
	ds_read_b128 v[150:153], v158 offset:1024
	ds_read_b128 v[154:157], v158 offset:2048
	ds_read_b128 v[158:161], v158 offset:3072
	ds_read_b128 v[162:165], v174
	ds_read_b128 v[166:169], v174 offset:1024
	ds_read_b128 v[170:173], v174 offset:2048
	ds_read_b128 v[174:177], v174 offset:3072
	s_add_u32 s48, s48, 0x100000
	s_addc_u32 s49, s49, 0
	s_mov_b32 m0, s61
	v_lshl_add_u64 v[236:237], s[48:49], 0, v[136:137]
	ds_read_b128 v[178:181], v196 offset:32768
	ds_read_b128 v[182:185], v196 offset:33792
	ds_read_b128 v[186:189], v196 offset:34816
	ds_read_b128 v[198:201], v196 offset:35840
	ds_read_b128 v[202:205], v196 offset:36864
	ds_read_b128 v[206:209], v196 offset:37888
	ds_read_b128 v[210:213], v196 offset:38912
	ds_read_b128 v[214:217], v196 offset:39936
	global_load_lds_dwordx4 v[236:237], off
	v_lshl_add_u64 v[236:237], s[48:49], 0, v[134:135]
	s_mov_b32 m0, s62
	s_nop 0
	global_load_lds_dwordx4 v[236:237], off
	s_waitcnt vmcnt(8)
	s_waitcnt lgkmcnt(0)
	s_barrier
	s_setprio 1
	s_waitcnt lgkmcnt(0)
	v_mfma_f32_16x16x32_bf16 v[128:131], v[146:149], v[178:181], v[128:131]
	v_mfma_f32_16x16x32_bf16 v[124:127], v[154:157], v[178:181], v[124:127]
	v_mfma_f32_16x16x32_bf16 v[112:115], v[146:149], v[186:189], v[112:115]
	v_mfma_f32_16x16x32_bf16 v[108:111], v[154:157], v[186:189], v[108:111]
	v_mfma_f32_16x16x32_bf16 v[96:99], v[146:149], v[202:205], v[96:99]
	v_mfma_f32_16x16x32_bf16 v[92:95], v[154:157], v[202:205], v[92:95]
	v_mfma_f32_16x16x32_bf16 v[80:83], v[146:149], v[210:213], v[80:83]
	v_mfma_f32_16x16x32_bf16 v[76:79], v[154:157], v[210:213], v[76:79]
	v_mfma_f32_16x16x32_bf16 v[128:131], v[150:153], v[182:185], v[128:131]
	v_mfma_f32_16x16x32_bf16 v[124:127], v[158:161], v[182:185], v[124:127]
	v_mfma_f32_16x16x32_bf16 v[112:115], v[150:153], v[198:201], v[112:115]
	v_mfma_f32_16x16x32_bf16 v[108:111], v[158:161], v[198:201], v[108:111]
	v_mfma_f32_16x16x32_bf16 v[96:99], v[150:153], v[206:209], v[96:99]
	v_mfma_f32_16x16x32_bf16 v[92:95], v[158:161], v[206:209], v[92:95]
	v_mfma_f32_16x16x32_bf16 v[80:83], v[150:153], v[214:217], v[80:83]
	v_mfma_f32_16x16x32_bf16 v[76:79], v[158:161], v[214:217], v[76:79]
	s_setprio 0
	s_setprio 1
	v_mfma_f32_16x16x32_bf16 v[120:123], v[162:165], v[178:181], v[120:123]
	v_mfma_f32_16x16x32_bf16 v[116:119], v[170:173], v[178:181], v[116:119]
	v_mfma_f32_16x16x32_bf16 v[104:107], v[162:165], v[186:189], v[104:107]
	v_mfma_f32_16x16x32_bf16 v[100:103], v[170:173], v[186:189], v[100:103]
	v_mfma_f32_16x16x32_bf16 v[88:91], v[162:165], v[202:205], v[88:91]
	v_mfma_f32_16x16x32_bf16 v[84:87], v[170:173], v[202:205], v[84:87]
	v_mfma_f32_16x16x32_bf16 v[72:75], v[162:165], v[210:213], v[72:75]
	v_mfma_f32_16x16x32_bf16 v[68:71], v[170:173], v[210:213], v[68:71]
	v_mfma_f32_16x16x32_bf16 v[120:123], v[166:169], v[182:185], v[120:123]
	v_mfma_f32_16x16x32_bf16 v[116:119], v[174:177], v[182:185], v[116:119]
	v_mfma_f32_16x16x32_bf16 v[104:107], v[166:169], v[198:201], v[104:107]
	v_mfma_f32_16x16x32_bf16 v[100:103], v[174:177], v[198:201], v[100:103]
	v_mfma_f32_16x16x32_bf16 v[88:91], v[166:169], v[206:209], v[88:91]
	v_mfma_f32_16x16x32_bf16 v[84:87], v[174:177], v[206:209], v[84:87]
	v_mfma_f32_16x16x32_bf16 v[72:75], v[166:169], v[214:217], v[72:75]
	v_mfma_f32_16x16x32_bf16 v[68:71], v[174:177], v[214:217], v[68:71]
	s_setprio 0
	s_barrier
; #define PG8_STAGE(bufoff, gbase, voff) do { _Pragma("unroll") for (int _i = 0; _i < 2; ++_i) \
;         __builtin_amdgcn_global_load_lds((const unsigned*)((const char*)(gbase) + (voff)[_i]), (PG8_LAS unsigned*)(lds + (bufoff) + ldsw + _i * 8192), 16, 0, 0); } while (0)
; #define PG8_LDA(dst, b, h) do { _Pragma("unroll") for (int m = 0; m < 4; ++m) _Pragma("unroll") for (int k = 0; k < 2; ++k) dst[m][k] = *(const PG8_LAS bf16x8*)(lds + PG8_SA(b, h) + aoff + m * 2048 + k * 1024); } while (0)
; #define PG8_MMA(ai, bj, At, Bt) do { __builtin_amdgcn_s_setprio(1); _Pragma("unroll") for (int m = 0; m < 4; ++m) _Pragma("unroll") for (int n = 0; n < 2; ++n) _Pragma("unroll") for (int k = 0; k < 2; ++k) \
;         acc[ai][bj][m][n] = __builtin_amdgcn_mfma_f32_16x16x32_bf16(Bt[n][k], At[m][k], acc[ai][bj][m][n], 0, 0, 0); __builtin_amdgcn_s_setprio(0); } while (0)
; #define PG8_WAIT_V(n) asm volatile("s_waitcnt vmcnt(" #n ")" ::: "memory")
; #define PG8_WAIT_L(n) asm volatile("s_waitcnt lgkmcnt(" #n ")" ::: "memory")
; #define PG8_BAR __builtin_amdgcn_s_barrier()
; #define PG8_SCHED __builtin_amdgcn_sched_barrier(0)
;     __device__ __forceinline__ void operator()(const f32x4 (&acc)[2][2][4][2], const Unit& u, int wr, int wc, int fr, int fq) const {
;         const int seg = (u.pn + pn0) >> 2;
;         if (seg >= 13) run<3, 4>(acc, u, wr, wc, fr, fq);
;         else if (seg == 3 || seg == 7 || seg == 10 || seg == 12) run<1, 0>(acc, u, wr, wc, fr, fq);
; template <class Epi, class Sched, bool ALIGN_EPI = false, bool SP2 = false>
; __device__ __forceinline__ void gemm_phase(PG8_LAS unsigned char* lds, const Gemm g, const Sched& S, const Epi& E) {
;     ...
;             PG8_LDA(At, 1, 1); PG8_STAGE(PG8_SB(1, 0), b3, voffB); PG8_STAGE(PG8_SB(1, 1), b3 + hstep, voffB); PG8_STAGE(PG8_SA(1, 0), a3, voffA);
;             PG8_WAIT_V(8); PG8_WAIT_L(0); PG8_BAR; PG8_MMA(1, 0, At, B0); PG8_MMA(1, 1, At, B1); PG8_BAR; PG8_SCHED;
	s_add_i32 s48, s81, s58
	v_lshl_add_u64 v[194:195], v[194:195], 0, s[78:79]
	s_mov_b32 m0, s48
	ds_read_b128 v[178:181], v196 offset:49152
	ds_read_b128 v[182:185], v196 offset:50176
	ds_read_b128 v[186:189], v196 offset:51200
	ds_read_b128 v[198:201], v196 offset:52224
	ds_read_b128 v[202:205], v196 offset:53248
	ds_read_b128 v[206:209], v196 offset:54272
	ds_read_b128 v[210:213], v196 offset:55296
	ds_read_b128 v[214:217], v196 offset:56320
	global_load_lds_dwordx4 v[194:195], off
	s_add_i32 m0, s48, 0x2000
	s_add_u32 s46, s46, 0x100080
	v_lshl_add_u64 v[194:195], v[222:223], 0, s[78:79]
	s_addc_u32 s47, s47, 0
	s_add_i32 s48, s82, s58
	global_load_lds_dwordx4 v[194:195], off
	v_lshl_add_u64 v[194:195], s[46:47], 0, v[2:3]
	s_mov_b32 m0, s48
	s_nop 0
	global_load_lds_dwordx4 v[194:195], off
	v_lshl_add_u64 v[194:195], s[46:47], 0, v[132:133]
	s_add_i32 m0, s48, 0x2000
	s_nop 0
	global_load_lds_dwordx4 v[194:195], off
	v_lshl_add_u64 v[194:195], v[232:233], 0, s[78:79]
	s_mov_b32 m0, s66
	s_nop 0
	global_load_lds_dwordx4 v[194:195], off
	v_lshl_add_u64 v[194:195], v[234:235], 0, s[78:79]
	s_mov_b32 m0, s67
	s_nop 0
	global_load_lds_dwordx4 v[194:195], off
	s_waitcnt vmcnt(8)
	s_waitcnt lgkmcnt(0)
	s_barrier
	s_setprio 1
	s_waitcnt lgkmcnt(0)
	v_mfma_f32_16x16x32_bf16 v[64:67], v[146:149], v[178:181], v[64:67]
	v_mfma_f32_16x16x32_bf16 v[60:63], v[154:157], v[178:181], v[60:63]
	v_mfma_f32_16x16x32_bf16 v[48:51], v[146:149], v[186:189], v[48:51]
	v_mfma_f32_16x16x32_bf16 v[44:47], v[154:157], v[186:189], v[44:47]
	v_mfma_f32_16x16x32_bf16 v[32:35], v[146:149], v[202:205], v[32:35]
	v_mfma_f32_16x16x32_bf16 v[28:31], v[154:157], v[202:205], v[28:31]
	v_mfma_f32_16x16x32_bf16 v[16:19], v[146:149], v[210:213], v[16:19]
	v_mfma_f32_16x16x32_bf16 v[12:15], v[154:157], v[210:213], v[12:15]
	v_mfma_f32_16x16x32_bf16 v[64:67], v[150:153], v[182:185], v[64:67]
	v_mfma_f32_16x16x32_bf16 v[60:63], v[158:161], v[182:185], v[60:63]
	v_mfma_f32_16x16x32_bf16 v[48:51], v[150:153], v[198:201], v[48:51]
	v_mfma_f32_16x16x32_bf16 v[44:47], v[158:161], v[198:201], v[44:47]
	v_mfma_f32_16x16x32_bf16 v[32:35], v[150:153], v[206:209], v[32:35]
	v_mfma_f32_16x16x32_bf16 v[28:31], v[158:161], v[206:209], v[28:31]
	v_mfma_f32_16x16x32_bf16 v[16:19], v[150:153], v[214:217], v[16:19]
	v_mfma_f32_16x16x32_bf16 v[12:15], v[158:161], v[214:217], v[12:15]
	s_setprio 0
	s_setprio 1
	v_mfma_f32_16x16x32_bf16 v[56:59], v[162:165], v[178:181], v[56:59]
	v_mfma_f32_16x16x32_bf16 v[52:55], v[170:173], v[178:181], v[52:55]
	v_mfma_f32_16x16x32_bf16 v[40:43], v[162:165], v[186:189], v[40:43]
	v_mfma_f32_16x16x32_bf16 v[36:39], v[170:173], v[186:189], v[36:39]
	v_mfma_f32_16x16x32_bf16 v[24:27], v[162:165], v[202:205], v[24:27]
	v_mfma_f32_16x16x32_bf16 v[20:23], v[170:173], v[202:205], v[20:23]
	v_mfma_f32_16x16x32_bf16 v[8:11], v[162:165], v[210:213], v[8:11]
	v_mfma_f32_16x16x32_bf16 v[4:7], v[170:173], v[210:213], v[4:7]
	v_mfma_f32_16x16x32_bf16 v[56:59], v[166:169], v[182:185], v[56:59]
	v_mfma_f32_16x16x32_bf16 v[52:55], v[174:177], v[182:185], v[52:55]
	v_mfma_f32_16x16x32_bf16 v[40:43], v[166:169], v[198:201], v[40:43]
	v_mfma_f32_16x16x32_bf16 v[36:39], v[174:177], v[198:201], v[36:39]
	v_mfma_f32_16x16x32_bf16 v[24:27], v[166:169], v[206:209], v[24:27]
	v_mfma_f32_16x16x32_bf16 v[20:23], v[174:177], v[206:209], v[20:23]
	v_mfma_f32_16x16x32_bf16 v[8:11], v[166:169], v[214:217], v[8:11]
	v_mfma_f32_16x16x32_bf16 v[4:7], v[174:177], v[214:217], v[4:7]
	s_setprio 0
	s_barrier
	s_add_i32 s80, s80, 2
	s_add_u32 s12, s12, 0x100
	s_addc_u32 s13, s13, 0
	s_add_u32 s52, s52, 0x100
	s_addc_u32 s53, s53, 0
	s_cmp_gt_u32 s80, 61
	s_cbranch_scc0 .LBB0_153
	s_and_b64 vcc, exec, s[34:35]
	s_cbranch_vccnz .LBB0_164
	s_ashr_i32 s39, s1, 2
	s_cmp_lt_i32 s39, 13
	s_mov_b64 s[12:13], -1
	s_cbranch_scc1 .LBB0_165
